# attention-embedded layer-1 weight staging with trimmed per-step control (out-of-line rare paths, running VGPR offsets); 6 staging waves per CU; output projection one unit on every CU
# speedup vs baseline: 1.0125x; 1.0125x over previous
; #define LAS __attribute__((address_space(3)))
; #define WAIT_BAR(N) asm volatile("s_waitcnt vmcnt(" #N ") lgkmcnt(0)\n\ts_barrier" ::: "memory")
; #define DMA_K(t, slot) do { const bf16_t* sb_ = Kh + (long)(t) * KVBLK * DMK; glds16<0>(sb_, kvoff, (unsigned)__builtin_amdgcn_readfirstlane(kdst + (slot))); glds16<0>(sb_ + 64, kvoff, (unsigned)__builtin_amdgcn_readfirstlane(kdst + 8192 + (slot))); } while (0)
; template <int THRL> ...
;     ...
;   const bf16_t* Qw = Q + (size_t)(CTXL + qb * 128 + wq * QBLK) * DMK + head * 128 + comp * 64;
;   const bf16_t* Kh = K + head * 128; const bf16_t* Vh = V + head * 128;
;   const unsigned lds0 = (unsigned)(uintptr_t)shm;
;   LAS float* wsf = (LAS float*)(shm + LDS_WS) + wid * 64;
;   const unsigned kvoff = (unsigned)(lane * DMK + wid * 8) * 2u;
;   const unsigned vvoff = (unsigned)((16 * (wid & 3) + (lane >> 2)) * DMK + (wid >> 2) * 32 + (lane & 3) * 8) * 2u;
;   const unsigned kdst = lds0 + LDS_K + wid * 1024, vdst = lds0 + LDS_V + wid * 1024;
;     ...
;   const int vb0 = (int)(lds0 + LDS_V) + ((lane >> 4) & 1) * 32 + (lane & 3) * 8 + (4 * hi + ((lane & 15) >> 2)) * 64;
;   bf16x8 kf[8];
;   const lds_cptr shm3 = (lds_cptr)shm; const lds_cptr kp0 = shm3 + LDS_K + comp * 8192 + hi * 1024 + r32 * 16;
;   const lds_cptr vp0 = shm3 + LDS_V + ((lane >> 4) & 1) * 32 + (lane & 3) * 8 + (4 * hi + ((lane & 15) >> 2)) * 64;
;   DMA_K(0, 0); DMA_V(0, 0); DMA_K(1, SLOTB);
;   bf16x8 qr[4];
; #pragma unroll
;   for (int d0 = 0; d0 < 4; ++d0) qr[d0] = *reinterpret_cast<const bf16x8*>(&Qw[(long)r32 * DMK + d0 * 16 + hi * 8]);
;   float mhat = 0.f, l_reg = 0.f; f32x16 o[4]; o[0] = f32x16{}; o[1] = f32x16{}; o[2] = f32x16{}; o[3] = f32x16{}; f32x16 negm = f32x16{}; asm volatile("" : "+v"(negm));
;   bool resc = false;
;     ...
;   f32x16 pA0, pA1, pB0, pB1;
;   int sl_prev = 0, sl_cur = 0, sl_next = SLOTB;
;     ...
;   DMA_K(2, 2 * SLOTB);
;   WAIT_BAR(6);
;   qkt(pA0, pA1, kp0, qr, negm); asm volatile("s_nop 15\n\ts_nop 7" : "+v"(pA0), "+v"(pA1));
;   const lds_cptr qp = shm3 + LDS_Q + wid * 4096 + lane * 16;
; #pragma unroll
;   for (int d0 = 0; d0 < 4; ++d0) *(LAS bf16x8*)(shm + LDS_Q + wid * 4096 + lane * 16 + d0 * 1024) = qr[d0];
;   START(pA0, pA1);
.LBB0_527:
	s_lshl_b32 s0, s28, 1
	s_and_b32 s0, s0, 0x700
	s_add_u32 s33, s26, s0
	s_addc_u32 s53, s27, 0
	s_bfe_u32 s41, s39, 0x20006
	s_lshl_b32 s0, s36, 4
	s_and_b32 s37, s0, 0xffffff80
	s_lshl_b32 s0, s41, 5
	s_or_b32 s0, s37, s0
	s_addk_i32 s0, 0x100
	s_ashr_i32 s1, s0, 31
	s_lshr_b32 s40, s39, 6
	s_lshr_b32 s42, s39, 8
	s_lshl_b64 s[0:1], s[0:1], 11
	s_add_u32 s0, s5, s0
	s_addc_u32 s1, s17, s1
	s_lshl_b32 s2, s36, 7
	s_and_b32 s14, s2, 0x380
	s_lshl_b32 s8, s14, 1
	s_add_u32 s0, s0, s8
	s_addc_u32 s1, s1, 0
	s_lshl_b32 s43, s42, 6
	s_lshl_b32 s2, s42, 7
	s_add_u32 s2, s0, s2
	s_addc_u32 s3, s1, 0
	s_add_u32 s20, s22, s8
	s_addc_u32 s21, s23, 0
	s_add_u32 s8, s24, s8
	s_addc_u32 s9, s25, 0
	s_lshl_b32 s0, s41, 15
	s_add_i32 s0, s0, s43
	v_add_u32_e32 v235, s0, v219
	s_lshl_b32 s0, s40, 10
	s_add_i32 s49, s0, 0
	s_and_b32 s1, s39, 0x3fffffc0
	s_lshl_b32 s38, s40, 4
	s_add_i32 s46, s49, 0xc000
	s_add_u32 s44, s20, 0x80
	v_add_u32_e32 v237, s38, v218
	s_mov_b32 s0, m0
	s_mov_b32 m0, s49
	s_nop 0
	global_load_lds_dwordx4 v237, s[20:21] offset:0
	s_mov_b32 m0, s0
	s_addc_u32 s45, s21, 0
	s_add_i32 s54, s49, 0x2000
	s_mov_b32 s0, m0
	s_mov_b32 m0, s54
	s_nop 0
	global_load_lds_dwordx4 v237, s[44:45] offset:0
	s_mov_b32 m0, s0
	s_add_u32 s50, s8, 0x80
	s_mov_b32 s0, m0
	s_mov_b32 m0, s46
	s_nop 0
	global_load_lds_dwordx4 v235, s[8:9] offset:0
	s_mov_b32 m0, s0
	s_addc_u32 s51, s9, 0
	s_add_i32 s45, s49, 0xe000
	s_mov_b32 s0, m0
	s_mov_b32 m0, s45
	s_nop 0
	global_load_lds_dwordx4 v235, s[50:51] offset:0
	s_mov_b32 m0, s0
	s_add_u32 s50, s20, 0x20000
	s_addc_u32 s51, s21, 0
	s_add_i32 s52, s49, 0x4000
	s_mov_b32 s0, m0
	s_mov_b32 m0, s52
	s_nop 0
	global_load_lds_dwordx4 v237, s[50:51] offset:0
	s_mov_b32 m0, s0
	s_add_u32 s56, s20, 0x20080
	s_addc_u32 s57, s21, 0
	s_add_i32 s51, s49, 0x6000
	s_mov_b32 s0, m0
	s_mov_b32 m0, s51
	s_nop 0
	global_load_lds_dwordx4 v237, s[56:57] offset:0
	s_mov_b32 m0, s0
	global_load_dwordx4 v[66:69], v229, s[2:3]
	global_load_dwordx4 v[70:73], v229, s[2:3] offset:32
	global_load_dwordx4 v[74:77], v229, s[2:3] offset:64
	global_load_dwordx4 v[78:81], v229, s[2:3] offset:96
	v_mov_b64_e32 v[48:49], v[32:33]
	s_add_u32 s2, s20, 0x40000
	v_mov_b64_e32 v[46:47], v[30:31]
	v_mov_b64_e32 v[44:45], v[28:29]
	v_mov_b64_e32 v[42:43], v[26:27]
	v_mov_b64_e32 v[40:41], v[24:25]
	v_mov_b64_e32 v[38:39], v[22:23]
	v_mov_b64_e32 v[36:37], v[20:21]
	v_mov_b64_e32 v[34:35], v[18:19]
	s_addc_u32 s3, s21, 0
	s_add_i32 s48, s49, 0x8000
	s_mov_b32 s0, m0
	s_mov_b32 m0, s48
	s_nop 0
	global_load_lds_dwordx4 v237, s[2:3] offset:0
	s_mov_b32 m0, s0
	s_add_u32 s2, s20, 0x40080
	s_addc_u32 s3, s21, 0
	s_add_i32 s47, s49, 0xa000
	s_mov_b32 s0, m0
	s_mov_b32 m0, s47
	s_nop 0
	global_load_lds_dwordx4 v237, s[2:3] offset:0
	s_mov_b32 m0, s0
	v_lshl_add_u32 v236, s42, 13, v221
	s_waitcnt vmcnt(6) lgkmcnt(0)
	s_barrier
	ds_read_b128 v[4:7], v236
	s_lshl_b32 s2, s40, 12
	v_add_u32_e32 v233, s2, v222
	s_lshl_b32 s1, s1, 2
	s_add_i32 s50, s1, 0
	s_add_i32 s50, s50, 0x18000
	s_add_u32 s2, s20, 0x60000
	s_addc_u32 s3, s21, 0
	v_mov_b32_e32 v3, v2
	v_mov_b32_e32 v12, v2
	v_mov_b32_e32 v13, v2
	s_movk_i32 s57, 0x4000
	s_mov_b32 s0, 0
	s_mov_b32 s55, 0x8000
	v_lshl_add_u32 v232, v217, 2, s50
	v_mov_b32_e32 v238, 0
	s_mov_b32 s56, -1
	s_waitcnt vmcnt(3) lgkmcnt(0)
	v_mfma_f32_32x32x16_bf16 v[50:65], v[4:7], v[66:69], v[34:49]
	ds_read_b128 v[4:7], v236 offset:512
	s_waitcnt lgkmcnt(0)
	v_mfma_f32_32x32x16_bf16 v[34:49], v[4:7], v[66:69], v[34:49]
	ds_read_b128 v[4:7], v236 offset:2048
	s_waitcnt vmcnt(2) lgkmcnt(0)
	v_mfma_f32_32x32x16_bf16 v[50:65], v[4:7], v[70:73], v[50:65]
	ds_read_b128 v[4:7], v236 offset:2560
	s_waitcnt lgkmcnt(0)
	v_mfma_f32_32x32x16_bf16 v[34:49], v[4:7], v[70:73], v[34:49]
	ds_read_b128 v[4:7], v236 offset:4096
	ds_read_b128 v[8:11], v236 offset:4608
	ds_read_b128 v[82:85], v236 offset:6656
	ds_read_b128 v[14:17], v236 offset:6144
	s_waitcnt vmcnt(1) lgkmcnt(3)
	v_mfma_f32_32x32x16_bf16 v[50:65], v[4:7], v[74:77], v[50:65]
	v_mov_b32_e32 v4, v2
	v_mov_b32_e32 v5, v2
	v_mov_b32_e32 v6, v2
	v_mov_b32_e32 v7, v2
	s_waitcnt lgkmcnt(2)
	v_mfma_f32_32x32x16_bf16 v[34:49], v[8:11], v[74:77], v[34:49]
	v_mov_b32_e32 v8, v2
	v_mov_b32_e32 v9, v2
	v_mov_b32_e32 v10, v2
	v_mov_b32_e32 v11, v2
	s_waitcnt vmcnt(0) lgkmcnt(0)
	v_mfma_f32_32x32x16_bf16 v[50:65], v[14:17], v[78:81], v[50:65]
	v_mov_b32_e32 v16, v2
	v_mov_b32_e32 v17, v2
	v_mov_b32_e32 v14, v2
	v_mov_b32_e32 v15, v2
	v_mfma_f32_32x32x16_bf16 v[34:49], v[82:85], v[78:81], v[34:49]
	s_nop 15
	s_nop 7
	ds_write_b128 v233, v[66:69]
	ds_write_b128 v233, v[70:73] offset:1024
	ds_write_b128 v233, v[74:77] offset:2048
	ds_write_b128 v233, v[78:81] offset:3072
	v_max3_f32 v66, v50, v51, v34
	v_max3_f32 v67, v52, v53, v35
	v_mov_b64_e32 v[96:97], v[16:17]
	v_max3_f32 v66, v66, v36, v37
	v_max3_f32 v67, v67, v56, v57
	v_mov_b64_e32 v[94:95], v[14:15]
	v_max3_f32 v66, v66, v54, v55
	v_max3_f32 v67, v67, v40, v41
	v_mov_b64_e32 v[92:93], v[12:13]
	v_max3_f32 v66, v66, v38, v39
	v_max3_f32 v67, v67, v60, v61
	v_mov_b64_e32 v[90:91], v[10:11]
	v_max3_f32 v66, v66, v58, v59
	v_max3_f32 v67, v67, v44, v45
	v_mov_b64_e32 v[88:89], v[8:9]
	v_max3_f32 v66, v66, v42, v43
	v_max3_f32 v67, v67, v64, v65
	v_mov_b64_e32 v[86:87], v[6:7]
	v_max3_f32 v66, v66, v62, v63
	v_max3_f32 v67, v67, v48, v49
	v_mov_b64_e32 v[84:85], v[4:5]
	v_max3_f32 v66, v66, v46, v47
	v_mov_b64_e32 v[82:83], v[2:3]
	v_max_f32_e32 v66, v66, v67
	s_nop 0
	v_mov_b32_e32 v67, v66
	s_nop 1
	v_permlane32_swap_b32_e32 v66, v67
	v_max_f32_e32 v66, v66, v67
	s_nop 0
	v_add_f32_e32 v234, v2, v66
	v_sub_f32_e32 v50, v50, v66
	v_sub_f32_e32 v34, v34, v66
	v_sub_f32_e32 v51, v51, v66
	v_sub_f32_e32 v35, v35, v66
	v_sub_f32_e32 v52, v52, v66
	s_nop 0
	v_xor_b32_e32 v98, 0x80000000, v234
	v_mov_b32_e32 v99, v98
	v_mov_b32_e32 v100, v98
	v_mov_b32_e32 v101, v98
	v_mov_b32_e32 v102, v98
	v_mov_b32_e32 v103, v98
	v_mov_b32_e32 v104, v98
	v_mov_b32_e32 v105, v98
	v_mov_b32_e32 v106, v98
	v_mov_b32_e32 v107, v98
	v_mov_b32_e32 v108, v98
	v_mov_b32_e32 v109, v98
	v_mov_b32_e32 v110, v98
	v_mov_b32_e32 v111, v98
	v_mov_b32_e32 v112, v98
	v_mov_b32_e32 v113, v98
	s_waitcnt vmcnt(0) lgkmcnt(0)
	s_barrier
; #define WAIT_BAR(N) asm volatile("s_waitcnt vmcnt(" #N ") lgkmcnt(0)\n\ts_barrier" ::: "memory")
; #define DMA_K(t, slot) do { const bf16_t* sb_ = Kh + (long)(t) * KVBLK * DMK; glds16<0>(sb_, kvoff, (unsigned)__builtin_amdgcn_readfirstlane(kdst + (slot))); glds16<0>(sb_ + 64, kvoff, (unsigned)__builtin_amdgcn_readfirstlane(kdst + 8192 + (slot))); } while (0)
; #define DMA_V(t, slot) do { const bf16_t* sb_ = Vh + (long)(t) * KVBLK * DMK; glds16<0>(sb_, vvoff, (unsigned)__builtin_amdgcn_readfirstlane(vdst + (slot))); glds16<0>(sb_ + 64, vvoff, (unsigned)__builtin_amdgcn_readfirstlane(vdst + 8192 + (slot))); } while (0)
; #define ROT() do { sl_prev = sl_cur; sl_cur = sl_next; sl_next = (sl_next == (NSLOT - 1) * SLOTB) ? 0 : sl_next + SLOTB; } while (0)
; template <int THRL> ...
;     ...
;   START(pA0, pA1);
; #pragma unroll
;   for (int r = 0; r < 16; ++r) pA1[r] = __builtin_amdgcn_exp2f(pA1[r]);
;   WAIT_BAR(0);
;   DMA_K(3, 0); DMA_V(1, SLOTB);
;   ROT();
;   kload8(kf, kp0 + sl_cur);
;   WAIT_BAR(4);
;   s16x4 vlo[4], vhi[4]; u32x4 pw0, pw1, pw2, pw3;
	s_mov_b32 s1, m0
	s_mov_b32 m0, s49
	s_nop 0
	global_load_lds_dwordx4 v237, s[2:3] offset:0
	s_mov_b32 m0, s1
	s_add_u32 s2, s20, 0x60080
	s_addc_u32 s3, s21, 0
	s_mov_b32 s1, m0
	s_mov_b32 m0, s54
	s_nop 0
	global_load_lds_dwordx4 v237, s[2:3] offset:0
	s_mov_b32 m0, s1
	s_add_u32 s2, s8, 0x20000
	s_addc_u32 s3, s9, 0
	s_add_i32 s44, s49, 0x10000
	s_mov_b32 s1, m0
	s_mov_b32 m0, s44
	s_nop 0
	global_load_lds_dwordx4 v235, s[2:3] offset:0
	s_mov_b32 m0, s1
	s_add_u32 s2, s8, 0x20080
	s_addc_u32 s3, s9, 0
	s_add_i32 s43, s49, 0x12000
	s_mov_b32 s1, m0
	s_mov_b32 m0, s43
	s_nop 0
	global_load_lds_dwordx4 v235, s[2:3] offset:0
	s_mov_b32 m0, s1
	ds_read_b128 v[146:149], v236 offset:16384
	ds_read_b128 v[202:205], v236 offset:16896
	ds_read_b128 v[206:209], v236 offset:18432
	ds_read_b128 v[190:193], v236 offset:18944
	ds_read_b128 v[198:201], v236 offset:20480
	ds_read_b128 v[186:189], v236 offset:20992
	ds_read_b128 v[182:185], v236 offset:22528
	ds_read_b128 v[178:181], v236 offset:23040
	v_sub_f32_e32 v36, v36, v66
	v_sub_f32_e32 v53, v53, v66
	v_sub_f32_e32 v37, v37, v66
	v_sub_f32_e32 v54, v54, v66
	v_sub_f32_e32 v38, v38, v66
	v_sub_f32_e32 v55, v55, v66
	v_sub_f32_e32 v39, v39, v66
	v_sub_f32_e32 v56, v56, v66
	v_sub_f32_e32 v40, v40, v66
	v_sub_f32_e32 v57, v57, v66
	v_sub_f32_e32 v41, v41, v66
	v_sub_f32_e32 v58, v58, v66
	v_sub_f32_e32 v42, v42, v66
	v_sub_f32_e32 v59, v59, v66
	v_sub_f32_e32 v43, v43, v66
	v_sub_f32_e32 v60, v60, v66
	v_sub_f32_e32 v44, v44, v66
	v_sub_f32_e32 v61, v61, v66
	v_sub_f32_e32 v45, v45, v66
	v_sub_f32_e32 v62, v62, v66
	v_sub_f32_e32 v46, v46, v66
	v_sub_f32_e32 v63, v63, v66
	v_sub_f32_e32 v47, v47, v66
	v_sub_f32_e32 v64, v64, v66
	v_sub_f32_e32 v48, v48, v66
	v_sub_f32_e32 v65, v65, v66
	v_sub_f32_e32 v49, v49, v66
	v_exp_f32_e32 v130, v50
	v_exp_f32_e32 v131, v51
	v_exp_f32_e32 v132, v52
	v_exp_f32_e32 v133, v53
	v_exp_f32_e32 v134, v54
	v_exp_f32_e32 v135, v55
	v_exp_f32_e32 v136, v56
	v_exp_f32_e32 v137, v57
	v_exp_f32_e32 v138, v58
	v_exp_f32_e32 v139, v59
	v_exp_f32_e32 v140, v60
	v_exp_f32_e32 v141, v61
	v_exp_f32_e32 v142, v62
	v_exp_f32_e32 v143, v63
	v_exp_f32_e32 v144, v64
	v_exp_f32_e32 v145, v65
	v_exp_f32_e32 v114, v34
	v_exp_f32_e32 v115, v35
	v_exp_f32_e32 v116, v36
	v_exp_f32_e32 v117, v37
	v_exp_f32_e32 v118, v38
	v_exp_f32_e32 v119, v39
	v_exp_f32_e32 v120, v40
	v_exp_f32_e32 v121, v41
	v_exp_f32_e32 v122, v42
	v_exp_f32_e32 v123, v43
	v_exp_f32_e32 v124, v44
	v_exp_f32_e32 v125, v45
	v_exp_f32_e32 v126, v46
	v_exp_f32_e32 v127, v47
	v_exp_f32_e32 v128, v48
	v_exp_f32_e32 v129, v49
	s_waitcnt vmcnt(4) lgkmcnt(0)
	s_barrier
	v_mov_b64_e32 v[80:81], v[16:17]
	v_mov_b64_e32 v[48:49], v[16:17]
	v_mov_b64_e32 v[64:65], v[16:17]
	v_mov_b64_e32 v[78:79], v[14:15]
	v_mov_b64_e32 v[76:77], v[12:13]
	v_mov_b64_e32 v[74:75], v[10:11]
	v_mov_b64_e32 v[72:73], v[8:9]
	v_mov_b64_e32 v[70:71], v[6:7]
	v_mov_b64_e32 v[68:69], v[4:5]
	v_mov_b64_e32 v[66:67], v[2:3]
	v_mov_b64_e32 v[46:47], v[14:15]
	v_mov_b64_e32 v[44:45], v[12:13]
	v_mov_b64_e32 v[42:43], v[10:11]
	v_mov_b64_e32 v[40:41], v[8:9]
	v_mov_b64_e32 v[38:39], v[6:7]
	v_mov_b64_e32 v[36:37], v[4:5]
	v_mov_b64_e32 v[34:35], v[2:3]
	v_mov_b64_e32 v[62:63], v[14:15]
	v_mov_b64_e32 v[60:61], v[12:13]
	v_mov_b64_e32 v[58:59], v[10:11]
	v_mov_b64_e32 v[56:57], v[8:9]
	v_mov_b64_e32 v[54:55], v[6:7]
	v_mov_b64_e32 v[52:53], v[4:5]
	v_mov_b64_e32 v[50:51], v[2:3]
	v_mov_b32_e32 v244, 0x23ee8
	ds_read2_b64 v[250:253], v244 offset1:1
	ds_read_b64 v[254:255], v244 offset:16
	s_waitcnt lgkmcnt(0)
	v_readfirstlane_b32 s68, v250
	v_readfirstlane_b32 s69, v251
	v_readfirstlane_b32 s70, v252
	v_readfirstlane_b32 s71, v253
	v_readfirstlane_b32 s72, v254
	v_readfirstlane_b32 s73, v255
	ds_read_b64 v[250:251], v244 offset:40
	s_waitcnt lgkmcnt(0)
	v_readfirstlane_b32 s74, v250
	v_readfirstlane_b32 s75, v251
	s_add_u32 s76, s74, 0x16530000
	s_addc_u32 s77, s75, 0
	s_add_u32 s74, s74, 0xa530000
	s_addc_u32 s75, s75, 0
	v_lshrrev_b32_e32 v25, 3, v214
	v_and_b32_e32 v28, 7, v214
	v_lshlrev_b32_e32 v33, 4, v28
	v_lshl_add_u32 v24, v25, 12, v33
	v_lshl_add_u32 v246, v25, 13, v33
	v_lshlrev_b32_e32 v29, 8, v28
	v_lshl_add_u32 v29, v25, 1, v29
	s_lshl_b32 s2, s40, 11
	s_cmp_lt_u32 s40, 6
	s_mov_b32 s3, 0x20800
	s_cselect_b32 s3, 0x20800, s3
	s_add_i32 s2, s2, s3
	v_add_u32_e32 v29, s2, v29
	v_add_u32_e32 v29, 32, v29
	v_lshl_add_u32 v32, v214, 3, s2
	s_mul_i32 s66, s96, 6
	s_add_i32 s66, s66, s40
	s_cmpk_lt_u32 s36, 0x100
	s_movk_i32 s67, 112
	s_cselect_b32 s67, 112, s67
	s_cselect_b32 s2, 0, 0x5400
	s_add_i32 s66, s66, s2
	s_cmp_lt_u32 s40, 6
	s_cselect_b32 s67, s67, 0
	s_add_i32 s90, s67, 6
	s_cmp_eq_u32 s67, 0
	s_cselect_b32 s90, -1, s90
	global_load_dword v249, v24, s[68:69]
	global_load_dword v249, v24, s[68:69]

.LBB0_529:
	v_mfma_f32_32x32x16_bf16 v[66:81], v[194:197], v[134:137], v[66:81]
	v_exp_f32_e32 v162, v162
	v_exp_f32_e32 v163, v163
	ds_read_b64_tr_b16 v[122:123], v16 offset:50176
	ds_read_b64_tr_b16 v[124:125], v16 offset:50688
	s_add_u32 s58, s33, 0xfef80000
	s_addc_u32 s59, s53, -1
	s_add_u32 s2, s33, 0xfefe0000
	s_addc_u32 s3, s53, -1
	s_add_i32 s60, s57, s49
	s_mov_b32 s61, m0
	s_mov_b32 m0, s60
	s_nop 0
	global_load_lds_dwordx4 v237, s[2:3] offset:0
	s_mov_b32 m0, s61
	v_mfma_f32_32x32x16_bf16 v[82:97], v[194:197], v[130:133], v[82:97]
	v_exp_f32_e32 v164, v164
	v_exp_f32_e32 v165, v165
	ds_read_b64_tr_b16 v[126:127], v16 offset:54272
	ds_read_b64_tr_b16 v[128:129], v16 offset:54784
	s_waitcnt lgkmcnt(6)
	v_mfma_f32_32x32x16_bf16 v[34:49], v[194:197], v[118:121], v[34:49]
	v_exp_f32_e32 v166, v166
	v_exp_f32_e32 v167, v167
	ds_read_b64_tr_b16 v[130:131], v16 offset:58368
	ds_read_b64_tr_b16 v[132:133], v16 offset:58880
	s_add_u32 s2, s33, 0xfefe0080
	s_addc_u32 s3, s53, -1
	s_add_i32 s60, s57, s54
	s_mov_b32 s61, m0
	s_mov_b32 m0, s60
	s_nop 0
	global_load_lds_dwordx4 v237, s[2:3] offset:0
	s_mov_b32 m0, s61
	s_waitcnt lgkmcnt(6)
	v_mfma_f32_32x32x16_bf16 v[50:65], v[194:197], v[114:117], v[50:65]
	v_exp_f32_e32 v168, v168
	v_exp_f32_e32 v169, v169
	ds_read_b64_tr_b16 v[118:119], v16 offset:62464
	ds_read_b64_tr_b16 v[120:121], v16 offset:62976
	v_add_u32_e32 v17, s55, v236
	ds_read_b128 v[114:117], v17
	ds_read_b128 v[178:181], v17 offset:512
	s_waitcnt lgkmcnt(8)
	v_mfma_f32_32x32x16_bf16 v[66:81], v[12:15], v[122:125], v[66:81]
	v_exp_f32_e32 v170, v170
	v_exp_f32_e32 v171, v171
	ds_read_b64_tr_b16 v[134:135], v16 offset:51200
	ds_read_b64_tr_b16 v[136:137], v16 offset:51712
	s_add_u32 s2, s33, 0x20000
	s_addc_u32 s3, s53, 0
	s_add_i32 s60, s55, s46
	s_mov_b32 s61, m0
	s_mov_b32 m0, s60
	s_nop 0
	global_load_lds_dwordx4 v235, s[2:3] offset:0
	s_mov_b32 m0, s61
	s_waitcnt lgkmcnt(8)
	v_mfma_f32_32x32x16_bf16 v[82:97], v[12:15], v[126:129], v[82:97]
	v_exp_f32_e32 v172, v172
	v_exp_f32_e32 v173, v173
	ds_read_b64_tr_b16 v[122:123], v16 offset:55296
	ds_read_b64_tr_b16 v[124:125], v16 offset:55808
	ds_read_b128 v[198:201], v17 offset:2048
	ds_read_b128 v[186:189], v17 offset:2560
	s_waitcnt lgkmcnt(10)
	v_mfma_f32_32x32x16_bf16 v[34:49], v[12:15], v[130:133], v[34:49]
	v_exp_f32_e32 v174, v174
	v_exp_f32_e32 v175, v175
	ds_read_b64_tr_b16 v[126:127], v16 offset:59392
	ds_read_b64_tr_b16 v[128:129], v16 offset:59904
	s_add_u32 s2, s33, 0x20080
	s_addc_u32 s3, s53, 0
	s_add_i32 s60, s55, s45
	s_mov_b32 s61, m0
	s_mov_b32 m0, s60
	s_nop 0
	global_load_lds_dwordx4 v235, s[2:3] offset:0
	s_mov_b32 m0, s61
	s_waitcnt lgkmcnt(10)
	v_mfma_f32_32x32x16_bf16 v[50:65], v[12:15], v[118:121], v[50:65]
	v_exp_f32_e32 v176, v176
	v_exp_f32_e32 v177, v177
	ds_read_b64_tr_b16 v[130:131], v16 offset:63488
	ds_read_b64_tr_b16 v[132:133], v16 offset:64000
	ds_read_b128 v[206:209], v17 offset:4096
	ds_read_b128 v[190:193], v17 offset:4608
	s_waitcnt lgkmcnt(10)
	v_mfma_f32_32x32x16_bf16 v[66:81], v[8:11], v[134:137], v[66:81]
	v_exp_f32_e32 v146, v146
	v_exp_f32_e32 v147, v147
	ds_read_b64_tr_b16 v[118:119], v16 offset:52224
	ds_read_b64_tr_b16 v[120:121], v16 offset:52736
	s_waitcnt lgkmcnt(10)
	v_mfma_f32_32x32x16_bf16 v[82:97], v[8:11], v[122:125], v[82:97]
	v_exp_f32_e32 v148, v148
	v_exp_f32_e32 v149, v149
	ds_read_b64_tr_b16 v[134:135], v16 offset:56320
	ds_read_b64_tr_b16 v[136:137], v16 offset:56832
	ds_read_b128 v[202:205], v17 offset:6144
	ds_read_b128 v[182:185], v17 offset:6656
	s_waitcnt lgkmcnt(10)
	v_mfma_f32_32x32x16_bf16 v[34:49], v[8:11], v[126:129], v[34:49]
	v_exp_f32_e32 v150, v150
	v_exp_f32_e32 v151, v151
	ds_read_b64_tr_b16 v[122:123], v16 offset:60416
	ds_read_b64_tr_b16 v[124:125], v16 offset:60928
	s_waitcnt lgkmcnt(10)
	v_mfma_f32_32x32x16_bf16 v[50:65], v[8:11], v[130:133], v[50:65]
	v_exp_f32_e32 v152, v152
	v_exp_f32_e32 v153, v153
	ds_read_b64_tr_b16 v[126:127], v16 offset:64512
	ds_read_b64_tr_b16 v[128:129], v16 offset:65024
	s_waitcnt lgkmcnt(8)
	v_mfma_f32_32x32x16_bf16 v[66:81], v[4:7], v[118:121], v[66:81]
	v_exp_f32_e32 v154, v154
	v_exp_f32_e32 v155, v155
	s_add_i32 s2, s56, 1
	s_cmp_gt_i32 s2, s90
	s_cbranch_scc1 .Lcs_done_h0
	s_waitcnt vmcnt(6)
	v_cvt_pk_bf16_f32 v245, v250, v251
	v_cvt_pk_bf16_f32 v244, v252, v253
	s_cmp_lt_u32 s2, 7
	s_cbranch_scc1 .Lcs_dumS_h0
	s_bitcmp1_b32 s2, 1
	s_cbranch_scc1 .Lcs_Sb_h0
	global_store_dwordx2 v28, v[30:31], s[100:101] nt
	v_add_u32_e32 v28, s63, v28
.Lcs_noS_h0:
	s_cmp_ge_u32 s2, s67
	s_cbranch_scc1 .Lcs_dumL_h0
	s_and_b32 s61, s2, 7
	s_cmp_eq_u32 s61, 0
	s_cbranch_scc1 .Lcs_dec_h0
.Lcs_Lgo_h0:
	global_load_dwordx4 v[250:253], v25, s[98:99] nt
	v_add_u32_e32 v25, s62, v25
.Lcs_noL_h0:
	s_waitcnt lgkmcnt(6)
	v_mfma_f32_32x32x16_bf16 v[82:97], v[4:7], v[134:137], v[82:97]
	v_exp_f32_e32 v156, v156
	v_exp_f32_e32 v157, v157
	s_waitcnt lgkmcnt(2)
	v_mfma_f32_32x32x16_bf16 v[34:49], v[4:7], v[122:125], v[34:49]
	v_exp_f32_e32 v158, v158
	v_exp_f32_e32 v159, v159
	s_waitcnt lgkmcnt(0)
	v_mfma_f32_32x32x16_bf16 v[50:65], v[4:7], v[126:129], v[50:65]
	v_exp_f32_e32 v160, v160
	v_exp_f32_e32 v161, v161
	s_waitcnt lgkmcnt(0)
	s_cmp_gt_i32 s2, s90
	s_cbranch_scc1 .Lcs_noW_h0
	s_bitcmp1_b32 s2, 1
	s_cbranch_scc1 .Lcs_R_h0
.Lcs_W_h0:
	ds_write_b16 v29, v245
	ds_write_b16_d16_hi v29, v245 offset:64
	ds_write_b16 v29, v244 offset:128
	ds_write_b16_d16_hi v29, v244 offset:192
	v_add_u32_e32 v29, 16, v29

.LBB0_532:
	s_add_i32 s2, s55, 0x4000
	s_cmpk_lg_u32 s55, 0x8000
	s_cselect_b32 s57, s2, 0
	v_mfma_f32_32x32x16_bf16 v[66:81], v[194:197], v[166:169], v[66:81]
	v_exp_f32_e32 v130, v130
	v_exp_f32_e32 v131, v131
	ds_read_b64_tr_b16 v[154:155], v16 offset:50176
	ds_read_b64_tr_b16 v[156:157], v16 offset:50688
	s_add_u32 s2, s58, 0x80000
	s_addc_u32 s3, s59, 0
	s_add_i32 s60, s55, s49
	s_mov_b32 s61, m0
	s_mov_b32 m0, s60
	s_nop 0
	global_load_lds_dwordx4 v237, s[2:3] offset:0
	s_mov_b32 m0, s61
	v_mfma_f32_32x32x16_bf16 v[82:97], v[194:197], v[162:165], v[82:97]
	v_exp_f32_e32 v132, v132
	v_exp_f32_e32 v133, v133
	ds_read_b64_tr_b16 v[158:159], v16 offset:54272
	ds_read_b64_tr_b16 v[160:161], v16 offset:54784
	s_waitcnt lgkmcnt(6)
	v_mfma_f32_32x32x16_bf16 v[34:49], v[194:197], v[150:153], v[34:49]
	v_exp_f32_e32 v134, v134
	v_exp_f32_e32 v135, v135
	ds_read_b64_tr_b16 v[162:163], v16 offset:58368
	ds_read_b64_tr_b16 v[164:165], v16 offset:58880
	s_add_u32 s2, s58, 0x80080
	s_addc_u32 s3, s59, 0
	s_add_i32 s58, s55, s54
	s_mov_b32 s59, m0
	s_mov_b32 m0, s58
	s_nop 0
	global_load_lds_dwordx4 v237, s[2:3] offset:0
	s_mov_b32 m0, s59
	s_waitcnt lgkmcnt(6)
	v_mfma_f32_32x32x16_bf16 v[50:65], v[194:197], v[146:149], v[50:65]
	v_exp_f32_e32 v136, v136
	v_exp_f32_e32 v137, v137
	ds_read_b64_tr_b16 v[150:151], v16 offset:62464
	ds_read_b64_tr_b16 v[152:153], v16 offset:62976
	v_add_u32_e32 v3, s57, v236
	ds_read_b128 v[146:149], v3
	ds_read_b128 v[202:205], v3 offset:512
	s_waitcnt lgkmcnt(8)
	v_mfma_f32_32x32x16_bf16 v[66:81], v[12:15], v[154:157], v[66:81]
	v_exp_f32_e32 v138, v138
	v_exp_f32_e32 v139, v139
	ds_read_b64_tr_b16 v[166:167], v16 offset:51200
	ds_read_b64_tr_b16 v[168:169], v16 offset:51712
	s_add_u32 s2, s33, 0x40000
	s_addc_u32 s3, s53, 0
	s_add_i32 s58, s57, s46
	s_mov_b32 s59, m0
	s_mov_b32 m0, s58
	s_nop 0
	global_load_lds_dwordx4 v235, s[2:3] offset:0
	s_mov_b32 m0, s59
	s_waitcnt lgkmcnt(8)
	v_mfma_f32_32x32x16_bf16 v[82:97], v[12:15], v[158:161], v[82:97]
	v_exp_f32_e32 v140, v140
	v_exp_f32_e32 v141, v141
	ds_read_b64_tr_b16 v[154:155], v16 offset:55296
	ds_read_b64_tr_b16 v[156:157], v16 offset:55808
	ds_read_b128 v[206:209], v3 offset:2048
	ds_read_b128 v[190:193], v3 offset:2560
	s_waitcnt lgkmcnt(10)
	v_mfma_f32_32x32x16_bf16 v[34:49], v[12:15], v[162:165], v[34:49]
	v_exp_f32_e32 v142, v142
	v_exp_f32_e32 v143, v143
	ds_read_b64_tr_b16 v[158:159], v16 offset:59392
	ds_read_b64_tr_b16 v[160:161], v16 offset:59904
	s_add_u32 s2, s33, 0x40080
	s_addc_u32 s3, s53, 0
	s_add_i32 s58, s57, s45
	s_mov_b32 s59, m0
	s_mov_b32 m0, s58
	s_nop 0
	global_load_lds_dwordx4 v235, s[2:3] offset:0
	s_mov_b32 m0, s59
	s_waitcnt lgkmcnt(10)
	v_mfma_f32_32x32x16_bf16 v[50:65], v[12:15], v[150:153], v[50:65]
	v_exp_f32_e32 v144, v144
	v_exp_f32_e32 v145, v145
	ds_read_b64_tr_b16 v[162:163], v16 offset:63488
	ds_read_b64_tr_b16 v[164:165], v16 offset:64000
	ds_read_b128 v[198:201], v3 offset:4096
	ds_read_b128 v[186:189], v3 offset:4608
	s_waitcnt lgkmcnt(10)
	v_mfma_f32_32x32x16_bf16 v[66:81], v[8:11], v[166:169], v[66:81]
	v_exp_f32_e32 v114, v114
	v_exp_f32_e32 v115, v115
	ds_read_b64_tr_b16 v[150:151], v16 offset:52224
	ds_read_b64_tr_b16 v[152:153], v16 offset:52736
	s_waitcnt lgkmcnt(10)
	v_mfma_f32_32x32x16_bf16 v[82:97], v[8:11], v[154:157], v[82:97]
	v_exp_f32_e32 v116, v116
	v_exp_f32_e32 v117, v117
	ds_read_b64_tr_b16 v[166:167], v16 offset:56320
	ds_read_b64_tr_b16 v[168:169], v16 offset:56832
	ds_read_b128 v[182:185], v3 offset:6144
	ds_read_b128 v[178:181], v3 offset:6656
	s_waitcnt lgkmcnt(10)
	v_mfma_f32_32x32x16_bf16 v[34:49], v[8:11], v[158:161], v[34:49]
	v_exp_f32_e32 v118, v118
	v_exp_f32_e32 v119, v119
	ds_read_b64_tr_b16 v[154:155], v16 offset:60416
	ds_read_b64_tr_b16 v[156:157], v16 offset:60928
	s_waitcnt lgkmcnt(10)
	v_mfma_f32_32x32x16_bf16 v[50:65], v[8:11], v[162:165], v[50:65]
	v_exp_f32_e32 v120, v120
	v_exp_f32_e32 v121, v121
	ds_read_b64_tr_b16 v[158:159], v16 offset:64512
	ds_read_b64_tr_b16 v[160:161], v16 offset:65024
	s_waitcnt lgkmcnt(8)
	v_mfma_f32_32x32x16_bf16 v[66:81], v[4:7], v[150:153], v[66:81]
	v_exp_f32_e32 v122, v122
	v_exp_f32_e32 v123, v123
	s_add_i32 s2, s56, 2
	s_cmp_gt_i32 s2, s90
	s_cbranch_scc1 .Lcs_done_h1
	s_waitcnt vmcnt(6)
	v_cvt_pk_bf16_f32 v245, v18, v19
	v_cvt_pk_bf16_f32 v244, v20, v21
	s_cmp_lt_u32 s2, 7
	s_cbranch_scc1 .Lcs_dumS_h1
	s_and_b32 s61, s2, 7
	s_cmp_eq_u32 s61, 7
	s_cbranch_scc1 .Lcs_adopt_h1
.Lcs_Sgo_h1:
	s_bitcmp1_b32 s2, 1
	s_cbranch_scc1 .Lcs_Sb_h1
	global_store_dwordx2 v28, v[22:23], s[100:101] nt
	v_add_u32_e32 v28, s63, v28
.Lcs_noS_h1:
	s_cmp_ge_u32 s2, s67
	s_cbranch_scc1 .Lcs_dumL_h1
	global_load_dwordx4 v[18:21], v25, s[98:99] nt
	v_add_u32_e32 v25, s62, v25
.Lcs_noL_h1:
	s_waitcnt lgkmcnt(6)
	v_mfma_f32_32x32x16_bf16 v[82:97], v[4:7], v[166:169], v[82:97]
	v_exp_f32_e32 v124, v124
	v_exp_f32_e32 v125, v125
	s_waitcnt lgkmcnt(2)
	v_mfma_f32_32x32x16_bf16 v[34:49], v[4:7], v[154:157], v[34:49]
	v_exp_f32_e32 v126, v126
	v_exp_f32_e32 v127, v127
	s_waitcnt lgkmcnt(0)
	v_mfma_f32_32x32x16_bf16 v[50:65], v[4:7], v[158:161], v[50:65]
	v_exp_f32_e32 v128, v128
	v_exp_f32_e32 v129, v129
	s_waitcnt lgkmcnt(0)
	s_cmp_gt_i32 s2, s90
	s_cbranch_scc1 .Lcs_noW_h1
	ds_write_b16 v29, v245
	ds_write_b16_d16_hi v29, v245 offset:64
	ds_write_b16 v29, v244 offset:128
	ds_write_b16_d16_hi v29, v244 offset:192
	s_bitcmp1_b32 s2, 1
	s_cselect_b32 s3, 16, -48
	v_add_u32_e32 v29, s3, v29

; __device__ __forceinline__ void convert_moe_items(const Ctx& a, int layer, LAS unsigned char* lds, int it0, int it1, int widx, int nw, int wave, int lane) {
;     ...
;     for (;;) {
;         cvt_store(da, va, scr, lane);
;         it += 2 * nw; const bool ha = (it < it1);
;         if (ha) { da = decode(it); cvt_load(da, va, lane); }
;         if (!hb) break;
;         cvt_store(db, vb, scr, lane);
;         hb = (it + nw < it1);
;         if (hb) { db = decode(it + nw); cvt_load(db, vb, lane); }
;         if (!ha) break;
;     }
.Lcs_done_h0:
	s_waitcnt vmcnt(4)
	s_branch .Lcs_noL_h0
.Lcs_dumS_h0:
	global_load_dword v249, v24, s[68:69]
	s_branch .Lcs_noS_h0

; #define LAS __attribute__((address_space(3)))
; __device__ __forceinline__ unsigned pk2(float lo, float hi) { return f2bf(lo) | (f2bf(hi) << 16); }
;     __device__ __forceinline__ const float* x() const { return (const float*)ld(0); }
;     __device__ __forceinline__ const float* c() const { return (const float*)ld(1); }
; template <bool NT = true> __device__ __forceinline__ void cvt_store(const CvtItem& d, const f32x4 (&v)[8], LAS float* scr, int lane) {
;     const int rr = lane >> 3, c4 = (lane & 7) * 4;
; #pragma unroll
;     for (int q = 0; q < 8; ++q) { LAS float* t = scr + (8 * q + rr) * 33 + c4; t[0] = v[q].x; t[1] = v[q].y; t[2] = v[q].z; t[3] = v[q].w; }
;     asm volatile("s_waitcnt lgkmcnt(0)" ::: "memory");
;     const int c = lane & 7;
; #pragma unroll
;     for (int j = 0; j < 4; ++j) { const int n = (lane >> 3) + 8 * j; const LAS float* s = scr + (8 * c) * 33 + n;
;         u32x4 o; o.x = pk2(s[0 * 33], s[1 * 33]); o.y = pk2(s[2 * 33], s[3 * 33]); o.z = pk2(s[4 * 33], s[5 * 33]); o.w = pk2(s[6 * 33], s[7 * 33]);
;         const int ng = d.n0 + n, drow = d.row_off + (d.ilv ? ((ng >> 7) * 256 + (ng & 127)) : ng);
;         if (NT) __builtin_nontemporal_store(o, (u32x4*)(d.dst + (size_t)drow * d.K + d.k0 + 8 * c)); else *(u32x4*)(d.dst + (size_t)drow * d.K + d.k0 + 8 * c) = o; }
;     asm volatile("s_waitcnt lgkmcnt(0)" ::: "memory");
; __device__ __forceinline__ void convert_moe_items(const Ctx& a, int layer, LAS unsigned char* lds, int it0, int it1, int widx, int nw, int wave, int lane) {
;     ...
;     auto decode = [&](int it) { CvtItem d; const int e = it / PER_E; int r = it % PER_E; const size_t eo = ((size_t)layer * NE + e) * (size_t)DM * FE;
;         if (r < I_G)          { d.src = wg + eo; d.dst = WGU; d.N = FE; d.K = DM; d.row_off = e * 2048; d.ilv = 1; }
;         else if (r < 2 * I_G) { r -= I_G; d.src = wu + eo; d.dst = WGU; d.N = FE; d.K = DM; d.row_off = e * 2048 + 128; d.ilv = 1; }
;         else                  { r -= 2 * I_G; d.src = wd + eo; d.dst = WD; d.N = DM; d.K = FE; d.row_off = e * 2048; d.ilv = 0; }
;         const int nblk = d.N / 32; d.k0 = 64 * (r / nblk); d.n0 = 32 * (r % nblk); return d; };
.Lcs_Sb_h0:
	global_store_dwordx2 v28, v[26:27], s[100:101] nt
	v_subrev_u32_e32 v28, s87, v28
	s_branch .Lcs_noS_h0
.Lcs_dec_h0:
	s_mul_i32 s78, s66, 0xaaab
	s_lshr_b32 s78, s78, 27
	s_mul_i32 s79, s78, 0xc00
	s_sub_i32 s79, s66, s79
	s_addk_i32 s66, 0x600
	s_add_i32 s80, s78, 16
	s_lshl_b32 s80, s80, 23
	s_lshl_b32 s81, s78, 11
	s_cmpk_gt_u32 s79, 0x7ff
	s_cbranch_scc1 .Lcs_down_h0
	s_mov_b64 s[98:99], s[68:69]
	s_cmpk_gt_u32 s79, 0x3ff
	s_cbranch_scc0 .Lcs_gate_h0
	s_mov_b64 s[98:99], s[70:71]
	s_addk_i32 s81, 0x80
	s_addk_i32 s79, 0xfc00
.Lcs_gate_h0:
	s_add_u32 s98, s98, s80
	s_addc_u32 s99, s99, 0
	s_lshr_b32 s82, s79, 5
	s_lshl_b32 s82, s82, 6
	s_and_b32 s83, s79, 31
	s_lshl_b32 s83, s83, 5
	s_lshl_b32 s84, s82, 12
	s_lshl_b32 s85, s83, 2
	s_add_i32 s84, s84, s85
	s_add_u32 s98, s98, s84
	s_addc_u32 s99, s99, 0
	s_mov_b32 s62, 0x8000
	s_mov_b32 s88, 0x8000
	s_mov_b32 s89, 0x17fc0
	s_lshr_b32 s84, s83, 7
	s_lshl_b32 s84, s84, 8
	s_and_b32 s85, s83, 0x7f
	s_add_i32 s84, s84, s85
	s_add_i32 s84, s84, s81
	s_lshl_b32 s84, s84, 12
	s_lshl_b32 s85, s82, 1
	s_add_i32 s84, s84, s85
	s_add_u32 s64, s74, s84
	s_addc_u32 s65, s75, 0
	v_mov_b32_e32 v25, v24
	v_lshrrev_b32_e32 v33, 1, v246
	s_branch .Lcs_Lgo_h0
.Lcs_down_h0:
	s_addk_i32 s79, 0xf800
	s_add_u32 s98, s72, s80
	s_addc_u32 s99, s73, 0
	s_lshr_b32 s82, s79, 6
	s_lshl_b32 s82, s82, 6
	s_and_b32 s83, s79, 63
	s_lshl_b32 s83, s83, 5
	s_lshl_b32 s84, s82, 13
	s_lshl_b32 s85, s83, 2
	s_add_i32 s84, s84, s85
	s_add_u32 s98, s98, s84
	s_addc_u32 s99, s99, 0
	s_mov_b32 s62, 0x10000
	s_mov_b32 s88, 0x4000
	s_mov_b32 s89, 0xbfc0
	s_add_i32 s84, s81, s83
	s_lshl_b32 s84, s84, 11
	s_lshl_b32 s85, s82, 1
	s_add_i32 s84, s84, s85
	s_add_u32 s64, s76, s84
	s_addc_u32 s65, s77, 0
	v_mov_b32_e32 v25, v246
	v_lshrrev_b32_e32 v33, 1, v24
	s_branch .Lcs_Lgo_h0
.Lcs_R_h0:
	ds_read_b64 v[254:255], v32
	ds_read_b64 v[30:31], v32 offset:512
	ds_read_b64 v[22:23], v32 offset:1024
	ds_read_b64 v[26:27], v32 offset:1536
	s_branch .Lcs_W_h0

; #define LAS __attribute__((address_space(3)))
; __device__ __forceinline__ unsigned pk2(float lo, float hi) { return f2bf(lo) | (f2bf(hi) << 16); }
;     __device__ __forceinline__ const float* x() const { return (const float*)ld(0); }
;     __device__ __forceinline__ const float* c() const { return (const float*)ld(1); }
; template <bool NT = true> __device__ __forceinline__ void cvt_store(const CvtItem& d, const f32x4 (&v)[8], LAS float* scr, int lane) {
;     const int rr = lane >> 3, c4 = (lane & 7) * 4;
; #pragma unroll
;     for (int q = 0; q < 8; ++q) { LAS float* t = scr + (8 * q + rr) * 33 + c4; t[0] = v[q].x; t[1] = v[q].y; t[2] = v[q].z; t[3] = v[q].w; }
;     asm volatile("s_waitcnt lgkmcnt(0)" ::: "memory");
;     const int c = lane & 7;
; #pragma unroll
;     for (int j = 0; j < 4; ++j) { const int n = (lane >> 3) + 8 * j; const LAS float* s = scr + (8 * c) * 33 + n;
;         u32x4 o; o.x = pk2(s[0 * 33], s[1 * 33]); o.y = pk2(s[2 * 33], s[3 * 33]); o.z = pk2(s[4 * 33], s[5 * 33]); o.w = pk2(s[6 * 33], s[7 * 33]);
;         const int ng = d.n0 + n, drow = d.row_off + (d.ilv ? ((ng >> 7) * 256 + (ng & 127)) : ng);
;         if (NT) __builtin_nontemporal_store(o, (u32x4*)(d.dst + (size_t)drow * d.K + d.k0 + 8 * c)); else *(u32x4*)(d.dst + (size_t)drow * d.K + d.k0 + 8 * c) = o; }
;     asm volatile("s_waitcnt lgkmcnt(0)" ::: "memory");
.Lcs_Sb_h1:
	global_store_dwordx2 v28, v[254:255], s[100:101] nt
	v_add_u32_e32 v28, s63, v28
	s_branch .Lcs_noS_h1
.Lcs_adopt_h1:
	s_mov_b64 s[100:101], s[64:65]
	v_mov_b32_e32 v28, v33
	s_mov_b32 s63, s88
	s_mov_b32 s87, s89
	s_branch .Lcs_Sgo_h1
